# grid barrier: the 16th workgroup of an XCD to arrive also issues buffer_wbl2 (background L2 write-back before the last arriver's)
# baseline (speedup 1.0000x reference)
.LBB0_610:
	s_or_b64 exec, exec, s[8:9]
	v_cvt_f32_u32_e32 v4, v2
	s_waitcnt vmcnt(0)
	v_readfirstlane_b32 s6, v3
	v_sub_u32_e32 v3, 0, v2
	v_rcp_iflag_f32_e32 v4, v4
	v_add_u32_e32 v5, s6, v1
	v_mul_f32_e32 v4, 0x4f7ffffe, v4
	v_cvt_u32_f32_e32 v4, v4
	v_mul_lo_u32 v1, v3, v4
	v_mul_hi_u32 v1, v4, v1
	v_add_u32_e32 v1, v4, v1
	v_mul_hi_u32 v1, v5, v1
	v_mul_lo_u32 v3, v1, v2
	v_sub_u32_e32 v3, v5, v3
	v_add_u32_e32 v4, 1, v1
	v_cmp_ge_u32_e32 vcc, v3, v2
	s_nop 1
	v_cndmask_b32_e32 v1, v1, v4, vcc
	v_sub_u32_e32 v4, v3, v2
	v_cndmask_b32_e32 v3, v3, v4, vcc
	v_add_u32_e32 v4, 1, v1
	v_cmp_ge_u32_e32 vcc, v3, v2
	v_add_u32_e32 v3, 1, v5
	s_nop 0
	v_cndmask_b32_e32 v1, v1, v4, vcc
	v_mul_lo_u32 v4, v2, v1
	v_add_u32_e32 v2, v4, v2
	v_cmp_ne_u32_e32 vcc, v3, v2
	s_and_saveexec_b64 s[6:7], vcc
	s_xor_b64 s[6:7], exec, s[6:7]
	s_cbranch_execz .LBB0_624
	v_and_b32_e32 v0, 31, v3
	v_cmp_eq_u32_e32 vcc, 16, v0
	s_cbranch_vccz .Lewb_0
	buffer_wbl2 sc1
.Lewb_0:
	s_waitcnt lgkmcnt(0)
	v_mov_b32_e32 v0, 0x2000
	global_load_dword v0, v0, s[4:5] offset:1024 sc1
	s_add_u32 s12, s4, 0x2400
	s_addc_u32 s13, s5, 0
	s_waitcnt vmcnt(0)
	v_cmp_eq_u32_e32 vcc, v0, v1
	s_and_saveexec_b64 s[8:9], vcc
	s_cbranch_execz .LBB0_623
	s_add_u32 s10, s92, 0x4200
	s_addc_u32 s11, s93, 0
	s_mov_b32 s24, 1
	s_mov_b64 s[14:15], 0
	v_mov_b32_e32 v0, 0
	s_branch .LBB0_614

.LBB0_800:
	s_or_b64 exec, exec, s[10:11]
	v_cvt_f32_u32_e32 v4, v2
	s_waitcnt vmcnt(0)
	v_readfirstlane_b32 s8, v3
	v_sub_u32_e32 v3, 0, v2
	v_rcp_iflag_f32_e32 v4, v4
	v_add_u32_e32 v5, s8, v1
	v_mul_f32_e32 v4, 0x4f7ffffe, v4
	v_cvt_u32_f32_e32 v4, v4
	v_mul_lo_u32 v1, v3, v4
	v_mul_hi_u32 v1, v4, v1
	v_add_u32_e32 v1, v4, v1
	v_mul_hi_u32 v1, v5, v1
	v_mul_lo_u32 v3, v1, v2
	v_sub_u32_e32 v3, v5, v3
	v_add_u32_e32 v4, 1, v1
	v_cmp_ge_u32_e32 vcc, v3, v2
	s_nop 1
	v_cndmask_b32_e32 v1, v1, v4, vcc
	v_sub_u32_e32 v4, v3, v2
	v_cndmask_b32_e32 v3, v3, v4, vcc
	v_add_u32_e32 v4, 1, v1
	v_cmp_ge_u32_e32 vcc, v3, v2
	v_add_u32_e32 v3, 1, v5
	s_nop 0
	v_cndmask_b32_e32 v1, v1, v4, vcc
	v_mul_lo_u32 v4, v2, v1
	v_add_u32_e32 v2, v4, v2
	v_cmp_ne_u32_e32 vcc, v3, v2
	s_and_saveexec_b64 s[8:9], vcc
	s_xor_b64 s[8:9], exec, s[8:9]
	v_readlane_b32 s63, v251, 57
	s_cbranch_execz .LBB0_814
	v_and_b32_e32 v0, 31, v3
	v_cmp_eq_u32_e32 vcc, 16, v0
	s_cbranch_vccz .Lewb_1
	buffer_wbl2 sc1
.Lewb_1:
	s_waitcnt lgkmcnt(0)
	v_mov_b32_e32 v0, 0x2000
	global_load_dword v0, v0, s[6:7] offset:1024 sc1
	s_add_u32 s14, s6, 0x2400
	s_addc_u32 s15, s7, 0
	s_waitcnt vmcnt(0)
	v_cmp_eq_u32_e32 vcc, v0, v1
	s_and_saveexec_b64 s[10:11], vcc
	s_cbranch_execz .LBB0_813
	s_add_u32 s12, s92, 0x4200
	s_addc_u32 s13, s93, 0
	s_mov_b32 s26, 1
	s_mov_b64 s[16:17], 0
	v_mov_b32_e32 v0, 0
	s_branch .LBB0_804

.LBB0_876:
	s_or_b64 exec, exec, s[6:7]
	v_cvt_f32_u32_e32 v4, v2
	s_waitcnt vmcnt(0)
	v_readfirstlane_b32 s4, v3
	v_sub_u32_e32 v3, 0, v2
	v_rcp_iflag_f32_e32 v4, v4
	v_add_u32_e32 v5, s4, v1
	v_mul_f32_e32 v4, 0x4f7ffffe, v4
	v_cvt_u32_f32_e32 v4, v4
	v_mul_lo_u32 v1, v3, v4
	v_mul_hi_u32 v1, v4, v1
	v_add_u32_e32 v1, v4, v1
	v_mul_hi_u32 v1, v5, v1
	v_mul_lo_u32 v3, v1, v2
	v_sub_u32_e32 v3, v5, v3
	v_add_u32_e32 v4, 1, v1
	v_cmp_ge_u32_e32 vcc, v3, v2
	s_nop 1
	v_cndmask_b32_e32 v1, v1, v4, vcc
	v_sub_u32_e32 v4, v3, v2
	v_cndmask_b32_e32 v3, v3, v4, vcc
	v_add_u32_e32 v4, 1, v1
	v_cmp_ge_u32_e32 vcc, v3, v2
	v_add_u32_e32 v3, 1, v5
	s_nop 0
	v_cndmask_b32_e32 v1, v1, v4, vcc
	v_mul_lo_u32 v4, v2, v1
	v_add_u32_e32 v2, v4, v2
	v_cmp_ne_u32_e32 vcc, v3, v2
	s_and_saveexec_b64 s[4:5], vcc
	s_xor_b64 s[4:5], exec, s[4:5]
	s_cbranch_execz .LBB0_890
	v_and_b32_e32 v0, 31, v3
	v_cmp_eq_u32_e32 vcc, 16, v0
	s_cbranch_vccz .Lewb_2
	buffer_wbl2 sc1
.Lewb_2:
	s_waitcnt lgkmcnt(0)
	v_mov_b32_e32 v0, 0x2000
	global_load_dword v0, v0, s[2:3] offset:1024 sc1
	s_add_u32 s10, s2, 0x2400
	s_addc_u32 s11, s3, 0
	s_waitcnt vmcnt(0)
	v_cmp_eq_u32_e32 vcc, v0, v1
	s_and_saveexec_b64 s[6:7], vcc
	s_cbranch_execz .LBB0_889
	s_add_u32 s8, s92, 0x4200
	s_addc_u32 s9, s93, 0
	s_mov_b32 s22, 1
	s_mov_b64 s[12:13], 0
	v_mov_b32_e32 v0, 0
	s_branch .LBB0_880

.Lewb_3:
	s_waitcnt lgkmcnt(0)
	v_mov_b32_e32 v0, 0x2000
	global_load_dword v0, v0, s[4:5] offset:1024 sc1
	s_add_u32 s10, s4, 0x2400
	s_addc_u32 s11, s5, 0
	s_waitcnt vmcnt(0)
	v_cmp_eq_u32_e32 vcc, v0, v1
	s_and_saveexec_b64 s[8:9], vcc
	s_cbranch_execz .LBB0_978
	s_mov_b32 s22, 1
	s_mov_b64 s[12:13], 0
	s_branch .LBB0_969

.LBB0_1424:
	s_or_b64 exec, exec, s[10:11]
	v_cvt_f32_u32_e32 v4, v2
	s_waitcnt vmcnt(0)
	v_readfirstlane_b32 s8, v3
	v_sub_u32_e32 v3, 0, v2
	v_rcp_iflag_f32_e32 v4, v4
	v_add_u32_e32 v5, s8, v1
	v_mul_f32_e32 v4, 0x4f7ffffe, v4
	v_cvt_u32_f32_e32 v4, v4
	v_mul_lo_u32 v1, v3, v4
	v_mul_hi_u32 v1, v4, v1
	v_add_u32_e32 v1, v4, v1
	v_mul_hi_u32 v1, v5, v1
	v_mul_lo_u32 v3, v1, v2
	v_sub_u32_e32 v3, v5, v3
	v_add_u32_e32 v4, 1, v1
	v_cmp_ge_u32_e32 vcc, v3, v2
	s_nop 1
	v_cndmask_b32_e32 v1, v1, v4, vcc
	v_sub_u32_e32 v4, v3, v2
	v_cndmask_b32_e32 v3, v3, v4, vcc
	v_add_u32_e32 v4, 1, v1
	v_cmp_ge_u32_e32 vcc, v3, v2
	v_add_u32_e32 v3, 1, v5
	s_nop 0
	v_cndmask_b32_e32 v1, v1, v4, vcc
	v_mul_lo_u32 v4, v2, v1
	v_add_u32_e32 v2, v4, v2
	v_cmp_ne_u32_e32 vcc, v3, v2
	s_and_saveexec_b64 s[8:9], vcc
	s_xor_b64 s[8:9], exec, s[8:9]
	s_cbranch_execz .LBB0_1438
	v_and_b32_e32 v0, 31, v3
	v_cmp_eq_u32_e32 vcc, 16, v0
	s_cbranch_vccz .Lewb_4
	buffer_wbl2 sc1
.Lewb_4:
	s_waitcnt lgkmcnt(0)
	v_mov_b32_e32 v0, 0x2000
	global_load_dword v0, v0, s[4:5] offset:1024 sc1
	s_add_u32 s12, s4, 0x2400
	s_addc_u32 s13, s5, 0
	s_waitcnt vmcnt(0)
	v_cmp_eq_u32_e32 vcc, v0, v1
	s_and_saveexec_b64 s[10:11], vcc
	s_cbranch_execz .LBB0_1437
	s_mov_b32 s25, 1
	s_mov_b64 s[14:15], 0
	s_branch .LBB0_1428

.Lewb_5:
	s_waitcnt lgkmcnt(0)
	v_mov_b32_e32 v0, 0x2000
	global_load_dword v0, v0, s[6:7] offset:1024 sc1
	s_add_u32 s12, s6, 0x2400
	s_addc_u32 s13, s7, 0
	s_waitcnt vmcnt(0)
	v_cmp_eq_u32_e32 vcc, v0, v1
	s_and_saveexec_b64 s[10:11], vcc
	s_cbranch_execz .LBB0_1549
	s_mov_b32 s25, 1
	s_mov_b64 s[14:15], 0
	s_branch .LBB0_1540

.Lewb_6:
	s_waitcnt lgkmcnt(0)
	v_mov_b32_e32 v0, 0x2000
	global_load_dword v0, v0, s[4:5] offset:1024 sc1
	s_add_u32 s10, s4, 0x2400
	s_addc_u32 s11, s5, 0
	s_waitcnt vmcnt(0)
	v_cmp_eq_u32_e32 vcc, v0, v1
	s_and_saveexec_b64 s[8:9], vcc
	s_cbranch_execz .LBB0_1726
	s_mov_b32 s23, 1
	s_mov_b64 s[12:13], 0
	s_branch .LBB0_1717

.LBB0_2016:
	s_or_b64 exec, exec, s[12:13]
	v_cvt_f32_u32_e32 v4, v2
	s_waitcnt vmcnt(0)
	v_readfirstlane_b32 s6, v3
	v_sub_u32_e32 v3, 0, v2
	v_rcp_iflag_f32_e32 v4, v4
	v_add_u32_e32 v5, s6, v1
	v_mul_f32_e32 v4, 0x4f7ffffe, v4
	v_cvt_u32_f32_e32 v4, v4
	v_mul_lo_u32 v1, v3, v4
	v_mul_hi_u32 v1, v4, v1
	v_add_u32_e32 v1, v4, v1
	v_mul_hi_u32 v1, v5, v1
	v_mul_lo_u32 v3, v1, v2
	v_sub_u32_e32 v3, v5, v3
	v_add_u32_e32 v4, 1, v1
	v_cmp_ge_u32_e32 vcc, v3, v2
	s_nop 1
	v_cndmask_b32_e32 v1, v1, v4, vcc
	v_sub_u32_e32 v4, v3, v2
	v_cndmask_b32_e32 v3, v3, v4, vcc
	v_add_u32_e32 v4, 1, v1
	v_cmp_ge_u32_e32 vcc, v3, v2
	v_add_u32_e32 v3, 1, v5
	s_nop 0
	v_cndmask_b32_e32 v1, v1, v4, vcc
	v_mul_lo_u32 v4, v2, v1
	v_add_u32_e32 v2, v4, v2
	v_cmp_ne_u32_e32 vcc, v3, v2
	s_and_saveexec_b64 s[6:7], vcc
	s_xor_b64 s[6:7], exec, s[6:7]
	s_cbranch_execz .LBB0_2030
	v_and_b32_e32 v0, 31, v3
	v_cmp_eq_u32_e32 vcc, 16, v0
	s_cbranch_vccz .Lewb_9
	buffer_wbl2 sc1
.Lewb_9:
	s_waitcnt lgkmcnt(0)
	v_mov_b32_e32 v0, 0x2000
	global_load_dword v0, v0, s[4:5] offset:1024 sc1
	s_add_u32 s14, s4, 0x2400
	s_addc_u32 s15, s5, 0
	s_waitcnt vmcnt(0)
	v_cmp_eq_u32_e32 vcc, v0, v1
	s_and_saveexec_b64 s[12:13], vcc
	s_cbranch_execz .LBB0_2029
	s_mov_b32 s26, 1
	s_mov_b64 s[16:17], 0
	s_branch .LBB0_2020
